# v61 + redundant self-max instructions folded in the attention softmax max chain (5 fewer VALU per K tile)
# speedup vs baseline: 1.0044x; 1.0044x over previous
; template <int OFF> __device__ __forceinline__ bf16x8 k_read(int kb) { bf16x8 r; asm volatile("ds_read_b128 %0, %1 offset:%2" : "=&v"(r) : "v"(kb), "i"(OFF) : "memory"); return r; }
; #define QK_STEP(D, X, Y, NEXT, N) do { K_WAIT(N, X, Y); \
;         p0 = __builtin_amdgcn_mfma_f32_32x32x16_bf16(X, qr[D], p0, 0, 0, 0); p1 = __builtin_amdgcn_mfma_f32_32x32x16_bf16(Y, qr[D], p1, 0, 0, 0); \
;         if constexpr ((NEXT) < 12) { X = k_read<(NEXT) * 32>(kb); Y = k_read<R1 + (NEXT) * 32>(kb); } } while (0)
; __device__ __forceinline__ void partialSM(f32x16& p0, f32x16& p1, float& m_reg, float& mn, float& alpha) {
;     constexpr float C = SCALE * 1.4426950408889634f;
;     float pmax = p0[0];
; #pragma unroll
;     for (int r = 1; r < 16; ++r) pmax = fmaxf(pmax, p0[r]);
; #pragma unroll
;     for (int r = 0; r < 16; ++r) pmax = fmaxf(pmax, p1[r]);
;     { auto rr = __builtin_amdgcn_permlane32_swap(__float_as_uint(pmax), __float_as_uint(pmax), false, false);
;       pmax = fmaxf(__uint_as_float(rr[0]), __uint_as_float(rr[1])); }
;     if (__builtin_expect(__all(pmax - m_reg <= THR / SCALE), 1)) { mn = m_reg; alpha = 1.f; }
;     else { mn = fmaxf(m_reg, pmax); alpha = __builtin_amdgcn_exp2f((m_reg - mn) * C); m_reg = mn; }
; __device__ __forceinline__ void qkt(f32x16& p0, f32x16& p1, const unsigned char* Ks, const bf16x8* qr, int r32, int hi) {
;     const int kb = (int)(uintptr_t)Ks + r32 * KPITCH + hi * 16;
;     constexpr int R1 = 32 * KPITCH;
;     p0 = f32x16{}; p1 = f32x16{};
;     bf16x8 a0 = k_read<0>(kb), a1 = k_read<R1>(kb), a2 = k_read<32>(kb), a3 = k_read<R1 + 32>(kb), a4 = k_read<64>(kb), a5 = k_read<R1 + 64>(kb);
;     ...
;     QK_STEP(0, a0, a1, 3, 4); QK_STEP(1, a2, a3, 4, 4); QK_STEP(2, a4, a5, 5, 4);
;     QK_STEP(3, a0, a1, 6, 4); QK_STEP(4, a2, a3, 7, 4); QK_STEP(5, a4, a5, 8, 4);
;     QK_STEP(6, a0, a1, 9, 4); QK_STEP(7, a2, a3, 10, 4); QK_STEP(8, a4, a5, 11, 4);
;     QK_STEP(9, a0, a1, 12, 4); QK_STEP(10, a2, a3, 12, 2); QK_STEP(11, a4, a5, 12, 0);
.LBB0_1001:
	s_bitcmp1_b32 s0, 0
	s_cselect_b32 s49, 0x6400, 0
	s_cmp_lg_u32 0, -1
	s_cselect_b32 s0, 0, 0
	s_add_i32 s0, s0, s49
	v_add_u32_e32 v174, s0, v178
	ds_read_b128 v[64:67], v174 offset:0
	ds_read_b128 v[68:71], v174 offset:0x3200
	ds_read_b128 v[180:183], v174 offset:32
	ds_read_b128 v[184:187], v174 offset:0x3220
	ds_read_b128 v[188:191], v174 offset:64
	ds_read_b128 v[192:195], v174 offset:0x3240
	s_nop 0
	s_waitcnt lgkmcnt(4)
	ds_read_b128 v[196:199], v174 offset:0x60
	ds_read_b128 v[200:203], v174 offset:0x3260
	s_waitcnt lgkmcnt(4)
	s_nop 0
	v_mfma_f32_32x32x16_bf16 v[80:95], v[64:67], v[142:145], 0
	v_mfma_f32_32x32x16_bf16 v[64:79], v[68:71], v[142:145], 0
	v_mfma_f32_32x32x16_bf16 v[80:95], v[180:183], v[138:141], v[80:95]
	ds_read_b128 v[180:183], v174 offset:0x80
	v_mfma_f32_32x32x16_bf16 v[64:79], v[184:187], v[138:141], v[64:79]
	ds_read_b128 v[184:187], v174 offset:0x3280
	s_waitcnt lgkmcnt(4)
	s_nop 0
	v_mfma_f32_32x32x16_bf16 v[80:95], v[188:191], v[134:137], v[80:95]
	ds_read_b128 v[188:191], v174 offset:0xa0
	v_mfma_f32_32x32x16_bf16 v[64:79], v[192:195], v[134:137], v[64:79]
	ds_read_b128 v[192:195], v174 offset:0x32a0
	s_waitcnt lgkmcnt(4)
	s_nop 0
	v_mfma_f32_32x32x16_bf16 v[80:95], v[196:199], v[130:133], v[80:95]
	ds_read_b128 v[196:199], v174 offset:0xc0
	v_mfma_f32_32x32x16_bf16 v[64:79], v[200:203], v[130:133], v[64:79]
	ds_read_b128 v[200:203], v174 offset:0x32c0
	s_waitcnt lgkmcnt(4)
	s_nop 0
	v_mfma_f32_32x32x16_bf16 v[80:95], v[180:183], v[126:129], v[80:95]
	ds_read_b128 v[180:183], v174 offset:0xe0
	v_mfma_f32_32x32x16_bf16 v[64:79], v[184:187], v[126:129], v[64:79]
	ds_read_b128 v[184:187], v174 offset:0x32e0
	s_waitcnt lgkmcnt(4)
	s_nop 0
	v_mfma_f32_32x32x16_bf16 v[80:95], v[188:191], v[122:125], v[80:95]
	ds_read_b128 v[188:191], v174 offset:0x100
	v_mfma_f32_32x32x16_bf16 v[64:79], v[192:195], v[122:125], v[64:79]
	ds_read_b128 v[192:195], v174 offset:0x3300
	s_waitcnt lgkmcnt(4)
	s_nop 0
	v_mfma_f32_32x32x16_bf16 v[80:95], v[196:199], v[118:121], v[80:95]
	ds_read_b128 v[196:199], v174 offset:0x120
	v_mfma_f32_32x32x16_bf16 v[64:79], v[200:203], v[118:121], v[64:79]
	ds_read_b128 v[200:203], v174 offset:0x3320
	s_waitcnt lgkmcnt(4)
	s_nop 0
	v_mfma_f32_32x32x16_bf16 v[80:95], v[180:183], v[114:117], v[80:95]
	ds_read_b128 v[180:183], v174 offset:0x140
	v_mfma_f32_32x32x16_bf16 v[64:79], v[184:187], v[114:117], v[64:79]
	ds_read_b128 v[184:187], v174 offset:0x3340
	s_waitcnt lgkmcnt(4)
	s_nop 0
	v_mfma_f32_32x32x16_bf16 v[80:95], v[188:191], v[110:113], v[80:95]
	ds_read_b128 v[188:191], v174 offset:0x160
	v_mfma_f32_32x32x16_bf16 v[64:79], v[192:195], v[110:113], v[64:79]
	ds_read_b128 v[192:195], v174 offset:0x3360
	s_waitcnt lgkmcnt(4)
	s_waitcnt lgkmcnt(2)
	s_nop 0
	s_waitcnt lgkmcnt(0)
	v_add_u32_e32 v207, s49, v172
	ds_read_b64_tr_b16 v[220:221], v207 offset:0
	ds_read_b64_tr_b16 v[222:223], v207 offset:1600
	ds_read_b64_tr_b16 v[224:225], v207 offset:64
	ds_read_b64_tr_b16 v[226:227], v207 offset:1664
	ds_read_b64_tr_b16 v[228:229], v207 offset:128
	ds_read_b64_tr_b16 v[230:231], v207 offset:1728
	ds_read_b64_tr_b16 v[232:233], v207 offset:192
	ds_read_b64_tr_b16 v[234:235], v207 offset:1792
	ds_read_b64_tr_b16 v[236:237], v207 offset:6400
	ds_read_b64_tr_b16 v[238:239], v207 offset:8000
	ds_read_b64_tr_b16 v[240:241], v207 offset:6464
	ds_read_b64_tr_b16 v[242:243], v207 offset:8064
	ds_read_b64_tr_b16 v[244:245], v207 offset:6528
	ds_read_b64_tr_b16 v[246:247], v207 offset:8128
	ds_read_b64_tr_b16 v[248:249], v207 offset:6592
	ds_read_b64_tr_b16 v[250:251], v207 offset:8192
	v_mfma_f32_32x32x16_bf16 v[80:95], v[196:199], v[106:109], v[80:95]
	v_mfma_f32_32x32x16_bf16 v[80:95], v[180:183], v[102:105], v[80:95]
	v_mfma_f32_32x32x16_bf16 v[64:79], v[200:203], v[106:109], v[64:79]
	v_mfma_f32_32x32x16_bf16 v[80:95], v[188:191], v[98:101], v[80:95]
	v_mfma_f32_32x32x16_bf16 v[64:79], v[184:187], v[102:105], v[64:79]
	s_nop 10
	v_max_f32_e32 v174, v80, v81
	v_max3_f32 v174, v174, v82, v83
	v_max3_f32 v174, v174, v84, v85
	v_max3_f32 v174, v174, v86, v87
	v_max3_f32 v174, v174, v88, v89
	v_mfma_f32_32x32x16_bf16 v[64:79], v[192:195], v[98:101], v[64:79]
	v_max3_f32 v174, v174, v90, v91
	v_max3_f32 v174, v174, v92, v93
	v_max3_f32 v174, v174, v94, v95
	s_nop 8
	v_max3_f32 v174, v174, v64, v65
	v_max3_f32 v174, v174, v66, v67
	v_max3_f32 v174, v174, v68, v69
	v_max3_f32 v174, v174, v70, v71
	v_max3_f32 v174, v174, v72, v73
	v_max3_f32 v174, v174, v74, v75
	v_max3_f32 v174, v174, v76, v77
	v_max3_f32 v174, v174, v78, v79
	v_mov_b32_e32 v180, v174
	s_nop 1
	v_permlane32_swap_b32_e32 v174, v180
	v_max_f32_e32 v174, v174, v180
	v_sub_f32_e32 v180, v174, v173
	v_max_f32_e32 v174, v173, v174
	v_sub_f32_e32 v181, v173, v174
	v_mul_f32_e32 v181, 0x3dd53b94, v181
	v_exp_f32_e32 v181, v181
	v_cmp_ge_f32_e32 vcc, s33, v180
	s_cmp_eq_u64 vcc, exec
	s_cselect_b64 s[38:39], -1, 0
	v_cndmask_b32_e64 v180, v181, 1.0, s[38:39]
	s_cbranch_scc1 .LBB0_1005
	s_and_saveexec_b64 s[0:1], s[36:37]
	ds_write_b32 v171, v180 offset:51328
	s_or_b64 exec, exec, s[0:1]
	s_waitcnt lgkmcnt(0)
	v_add_u32_e32 v181, v159, v96
	ds_read_b128 v[182:185], v181 offset:51424
	ds_read_b128 v[186:189], v181 offset:51392
	ds_read_b128 v[190:193], v181 offset:51360
	ds_read_b128 v[194:197], v181 offset:51328
	s_waitcnt lgkmcnt(3)
	v_pk_mul_f32 v[12:13], v[12:13], v[182:183]
	s_waitcnt lgkmcnt(2)
	v_pk_mul_f32 v[8:9], v[8:9], v[186:187]
	s_waitcnt lgkmcnt(1)
	v_pk_mul_f32 v[4:5], v[4:5], v[190:191]
	v_pk_mul_f32 v[14:15], v[14:15], v[184:185]
	v_pk_mul_f32 v[10:11], v[10:11], v[188:189]
	v_pk_mul_f32 v[6:7], v[6:7], v[192:193]
	s_waitcnt lgkmcnt(0)
	v_pk_mul_f32 v[2:3], v[2:3], v[196:197]
	v_pk_mul_f32 v[0:1], v[0:1], v[194:195]
	v_pk_mul_f32 v[60:61], v[60:61], v[182:183]
	v_pk_mul_f32 v[56:57], v[56:57], v[186:187]
	v_pk_mul_f32 v[52:53], v[52:53], v[190:191]
	v_pk_mul_f32 v[62:63], v[62:63], v[184:185]
	v_pk_mul_f32 v[58:59], v[58:59], v[188:189]
	v_pk_mul_f32 v[54:55], v[54:55], v[192:193]
	v_pk_mul_f32 v[50:51], v[50:51], v[196:197]
	v_pk_mul_f32 v[48:49], v[48:49], v[194:195]
	v_pk_mul_f32 v[44:45], v[44:45], v[182:183]
	v_pk_mul_f32 v[40:41], v[40:41], v[186:187]
	v_pk_mul_f32 v[36:37], v[36:37], v[190:191]
	v_pk_mul_f32 v[46:47], v[46:47], v[184:185]
	v_pk_mul_f32 v[42:43], v[42:43], v[188:189]
	v_pk_mul_f32 v[38:39], v[38:39], v[192:193]
	v_pk_mul_f32 v[34:35], v[34:35], v[196:197]
	v_pk_mul_f32 v[32:33], v[32:33], v[194:195]
	v_pk_mul_f32 v[28:29], v[28:29], v[182:183]
	v_pk_mul_f32 v[24:25], v[24:25], v[186:187]
	v_pk_mul_f32 v[20:21], v[20:21], v[190:191]
	v_pk_mul_f32 v[30:31], v[30:31], v[184:185]
	v_pk_mul_f32 v[26:27], v[26:27], v[188:189]
	v_pk_mul_f32 v[22:23], v[22:23], v[192:193]
	v_pk_mul_f32 v[18:19], v[18:19], v[196:197]
	v_pk_mul_f32 v[16:17], v[16:17], v[194:195]
